# stack11: stack9 plus RMS sum all-reduce via DPP in the router phase and gather-loop token records fetched up front with counted waits
# baseline (speedup 1.0000x reference)
; __device__ __forceinline__ float bflo(unsigned x) { return __uint_as_float(x << 16); }
; __device__ __forceinline__ float bfhi(unsigned x) { return __uint_as_float(x & 0xffff0000u); }
; __device__ __forceinline__ void phase_norm_route(const bf16_t* x, const float* g, const float* router, bf16_t* H, int* tok_info, unsigned* cnt, LAS unsigned char* lds, int tid, int wid, int lane) {
;     ...
;         for (int k = 0; k < 8; ++k) {
;             const int tl = wid * 8 + k, t = bt * 64 + tl;
;             u32x2 nxt[8]; { const int tn = t + (k < 7 ? 1 : 0);
; #pragma unroll
;               for (int j = 0; j < 8; ++j) nxt[j] = *(const u32x2*)(x + (size_t)tn * D + 4 * lane + 256 * j); }
;             f32x4 v[8]; { float ss = 0.f;
; #pragma unroll
;               for (int j = 0; j < 8; ++j) { const u32x2 w = raw[j]; v[j] = (f32x4){bflo(w.x), bfhi(w.x), bflo(w.y), bfhi(w.y)}; ss += (v[j][0] * v[j][0] + v[j][1] * v[j][1]) + (v[j][2] * v[j][2] + v[j][3] * v[j][3]); }
;               const float r = 1.0f / sqrtf(wave_sum(ss) * (1.0f / 2048.0f) + RMS_EPS);
.LBB0_2699:
	s_cmpk_lg_i32 s38, 0xe0
	s_cselect_b64 s[8:9], -1, 0
	v_cndmask_b32_e64 v18, 0, 1, s[8:9]
	v_mov_b32_e32 v19, s1
	v_lshl_add_u64 v[18:19], s[28:29], 0, v[18:19]
	v_lshlrev_b64 v[18:19], 12, v[18:19]
	s_waitcnt vmcnt(7) lgkmcnt(0)
	v_mov_b64_e32 v[16:17], v[108:109]
	v_lshl_add_u64 v[18:19], v[102:103], 0, v[18:19]
	s_waitcnt vmcnt(1)
	v_mov_b64_e32 v[4:5], v[122:123]
	v_mov_b64_e32 v[6:7], v[120:121]
	v_mov_b64_e32 v[8:9], v[118:119]
	v_mov_b64_e32 v[10:11], v[116:117]
	v_mov_b64_e32 v[12:13], v[114:115]
	v_mov_b64_e32 v[14:15], v[112:113]
	global_load_dwordx2 v[108:109], v[18:19], off
	global_load_dwordx2 v[112:113], v[18:19], off offset:512
	global_load_dwordx2 v[114:115], v[18:19], off offset:1024
	global_load_dwordx2 v[116:117], v[18:19], off offset:1536
	global_load_dwordx2 v[118:119], v[18:19], off offset:2048
	global_load_dwordx2 v[120:121], v[18:19], off offset:2560
	global_load_dwordx2 v[122:123], v[18:19], off offset:3072
	global_load_dwordx2 v[124:125], v[18:19], off offset:3584
	v_lshlrev_b32_e32 v18, 16, v16
	v_and_b32_e32 v19, 0xffff0000, v16
	v_lshlrev_b32_e32 v16, 16, v17
	v_and_b32_e32 v17, 0xffff0000, v17
	v_mul_f32_e32 v2, v17, v17
	v_pk_fma_f32 v[20:21], v[16:17], v[16:17], v[2:3] op_sel_hi:[1,1,0]
	v_lshlrev_b32_e32 v23, 16, v15
	v_lshlrev_b32_e32 v22, 16, v14
	v_and_b32_e32 v15, 0xffff0000, v15
	v_and_b32_e32 v14, 0xffff0000, v14
	v_mul_f32_e32 v2, v19, v19
	v_pk_mul_f32 v[24:25], v[14:15], v[14:15]
	v_lshlrev_b32_e32 v29, 16, v10
	v_pk_fma_f32 v[32:33], v[18:19], v[18:19], v[2:3] op_sel_hi:[1,1,0]
	v_pk_fma_f32 v[24:25], v[22:23], v[22:23], v[24:25]
	v_and_b32_e32 v31, 0xffff0000, v10
	v_mov_b32_e32 v28, v32
	v_mov_b32_e32 v34, v20
	v_mov_b32_e32 v35, v29
	v_and_b32_e32 v27, 0xffff0000, v12
	v_mul_f32_e32 v30, v31, v31
	v_pk_add_f32 v[20:21], v[32:33], v[20:21]
	v_pk_mul_f32 v[32:33], v[28:29], v[34:35]
	v_pk_add_f32 v[24:25], v[24:25], v[24:25] op_sel:[0,1] op_sel_hi:[1,0]
	v_lshlrev_b32_e32 v26, 16, v12
	v_lshlrev_b32_e32 v12, 16, v13
	v_and_b32_e32 v13, 0xffff0000, v13
	v_mov_b32_e32 v21, v33
	v_mov_b32_e32 v25, v30
	v_mul_f32_e32 v2, v27, v27
	v_lshlrev_b32_e32 v10, 16, v11
	v_and_b32_e32 v11, 0xffff0000, v11
	v_pk_add_f32 v[20:21], v[20:21], v[24:25]
	v_pk_fma_f32 v[24:25], v[26:27], v[26:27], v[2:3] op_sel_hi:[1,1,0]
	v_mul_f32_e32 v2, v13, v13
	v_mul_f32_e32 v68, v10, v10
	v_mul_f32_e32 v69, v11, v11
	v_pk_fma_f32 v[32:33], v[12:13], v[12:13], v[2:3] op_sel_hi:[1,1,0]
	v_mov_b32_e32 v25, v68
	v_mov_b32_e32 v33, v69
	v_pk_add_f32 v[24:25], v[24:25], v[32:33]
	v_lshlrev_b32_e32 v35, 16, v7
	v_pk_add_f32 v[20:21], v[20:21], v[24:25]
	v_lshlrev_b32_e32 v25, 16, v9
	v_lshlrev_b32_e32 v24, 16, v8
	v_and_b32_e32 v9, 0xffff0000, v9
	v_and_b32_e32 v8, 0xffff0000, v8
	v_pk_mul_f32 v[32:33], v[8:9], v[8:9]
	v_lshlrev_b32_e32 v34, 16, v6
	v_pk_fma_f32 v[32:33], v[24:25], v[24:25], v[32:33]
	v_and_b32_e32 v7, 0xffff0000, v7
	v_pk_add_f32 v[32:33], v[32:33], v[32:33] op_sel:[0,1] op_sel_hi:[1,0]
	v_and_b32_e32 v6, 0xffff0000, v6
	s_waitcnt vmcnt(8)
	v_lshlrev_b32_e32 v137, 16, v0
	v_pk_add_f32 v[20:21], v[20:21], v[20:21] op_sel:[0,1] op_sel_hi:[1,0]
	v_pk_mul_f32 v[68:69], v[6:7], v[6:7]
	v_mov_b32_e32 v136, v20
	v_mov_b32_e32 v72, v32
	v_mov_b32_e32 v73, v137
	v_pk_fma_f32 v[68:69], v[34:35], v[34:35], v[68:69]
	v_and_b32_e32 v139, 0xffff0000, v0
	v_pk_add_f32 v[20:21], v[20:21], v[32:33]
	v_pk_mul_f32 v[32:33], v[136:137], v[72:73]
	v_and_b32_e32 v71, 0xffff0000, v4
	v_mul_f32_e32 v2, v139, v139
	v_mov_b32_e32 v21, v33
	v_pk_add_f32 v[32:33], v[68:69], v[68:69] op_sel:[0,1] op_sel_hi:[1,0]
	v_lshlrev_b32_e32 v70, 16, v4
	v_lshlrev_b32_e32 v4, 16, v5
	v_and_b32_e32 v5, 0xffff0000, v5
	v_mov_b32_e32 v33, v2
	v_mul_f32_e32 v2, v71, v71
	v_lshlrev_b32_e32 v0, 16, v1
	v_and_b32_e32 v1, 0xffff0000, v1
	v_pk_add_f32 v[20:21], v[20:21], v[32:33]
	v_pk_fma_f32 v[32:33], v[70:71], v[70:71], v[2:3] op_sel_hi:[1,1,0]
	v_mul_f32_e32 v2, v5, v5
	v_mul_f32_e32 v28, v0, v0
	v_mul_f32_e32 v30, v1, v1
	v_pk_fma_f32 v[68:69], v[4:5], v[4:5], v[2:3] op_sel_hi:[1,1,0]
	v_mov_b32_e32 v33, v28
	v_mov_b32_e32 v69, v30
	v_pk_add_f32 v[32:33], v[32:33], v[68:69]
	v_mov_b32_e32 v138, v137
	v_pk_add_f32 v[20:21], v[20:21], v[32:33]
	s_nop 0
	v_add_f32_e32 v2, v20, v21
	s_waitcnt lgkmcnt(0)
; #define LAS __attribute__((address_space(3)))
; __device__ __forceinline__ float bflo(unsigned x) { return __uint_as_float(x << 16); }
; __device__ __forceinline__ float bfhi(unsigned x) { return __uint_as_float(x & 0xffff0000u); }
; __device__ __forceinline__ float wave_sum(float v) {
; #pragma unroll
;     for (int o = 1; o < 64; o <<= 1) v += __shfl_xor(v, o);
;     return v;
; __device__ __forceinline__ void phase_norm_route(const bf16_t* x, const float* g, const float* router, bf16_t* H, int* tok_info, unsigned* cnt, LAS unsigned char* lds, int tid, int wid, int lane) {
;     ...
;             f32x4 v[8]; { float ss = 0.f;
; #pragma unroll
;               for (int j = 0; j < 8; ++j) { const u32x2 w = raw[j]; v[j] = (f32x4){bflo(w.x), bfhi(w.x), bflo(w.y), bfhi(w.y)}; ss += (v[j][0] * v[j][0] + v[j][1] * v[j][1]) + (v[j][2] * v[j][2] + v[j][3] * v[j][3]); }
;               const float r = 1.0f / sqrtf(wave_sum(ss) * (1.0f / 2048.0f) + RMS_EPS);
; #pragma unroll
;               for (int j = 0; j < 8; ++j) { v[j] = v[j] * r * gg[j]; raw[j] = nxt[j]; } }
;             { unsigned char* h8 = (unsigned char*)H + (size_t)t * D;
;               LAS unsigned char* img = lds + 69632 + wid * 9216;
; #pragma unroll
;               for (int j = 0; j < 8; ++j) *(LAS f32x4*)(img + ((lane >> 3) + 8 * j) * 144 + (lane & 7) * 16) = v[j];
;               asm volatile("s_waitcnt lgkmcnt(0)" ::: "memory");
;               pg8::v16f a, b;
; #pragma unroll
;               for (int q = 0; q < 4; ++q) { const f32x4 x = *(const LAS f32x4*)(img + lane * 144 + q * 16), y = *(const LAS f32x4*)(img + lane * 144 + 64 + q * 16);
; #pragma unroll
;                   for (int c = 0; c < 4; ++c) { a[4 * q + c] = x[c]; b[4 * q + c] = y[c]; } }
;               asm volatile("s_waitcnt lgkmcnt(0)" ::: "memory");
;               u32x4 w0, w1; pg8::mx6_block(a, b, 1.0f, w0, w1);
	s_nop 1
	v_add_f32_dpp v2, v2, v2 quad_perm:[1,0,3,2] row_mask:0xf bank_mask:0xf
	s_nop 1
	v_add_f32_dpp v2, v2, v2 quad_perm:[2,3,0,1] row_mask:0xf bank_mask:0xf
	s_nop 1
	v_add_f32_dpp v2, v2, v2 row_half_mirror row_mask:0xf bank_mask:0xf
	s_nop 1
	v_add_f32_dpp v2, v2, v2 row_mirror row_mask:0xf bank_mask:0xf
	v_mov_b32_e32 v20, v2
	s_nop 1
	v_permlane16_swap_b32_e32 v20, v2
	v_add_f32_e32 v2, v2, v20
	v_mov_b32_e32 v20, v2
	s_nop 1
	v_permlane32_swap_b32_e32 v20, v2
	v_add_f32_e32 v2, v2, v20
	v_fmamk_f32 v2, v2, 0x3a000000, v191
	v_cmp_gt_f32_e32 vcc, s39, v2
	v_mul_f32_e32 v20, 0x4f800000, v2
	s_nop 0
	v_cndmask_b32_e32 v2, v2, v20, vcc
	v_sqrt_f32_e32 v20, v2
	s_nop 0
	v_add_u32_e32 v21, -1, v20
	v_fma_f32 v28, -v21, v20, v2
	v_cmp_ge_f32_e64 s[8:9], 0, v28
	v_add_u32_e32 v28, 1, v20
	s_nop 0
	v_cndmask_b32_e64 v21, v20, v21, s[8:9]
	v_fma_f32 v20, -v28, v20, v2
	v_cmp_lt_f32_e64 s[8:9], 0, v20
	s_nop 1
	v_cndmask_b32_e64 v20, v21, v28, s[8:9]
	v_mul_f32_e32 v21, 0x37800000, v20
	v_cndmask_b32_e32 v20, v20, v21, vcc
	v_cmp_class_f32_e32 vcc, v2, v201
	s_nop 1
	v_cndmask_b32_e32 v2, v20, v2, vcc
	v_div_scale_f32 v20, s[8:9], v2, v2, 1.0
	v_rcp_f32_e32 v21, v20
	s_nop 0
	v_fma_f32 v28, -v20, v21, 1.0
	v_fmac_f32_e32 v21, v28, v21
	v_div_scale_f32 v28, vcc, 1.0, v2, 1.0
	v_mul_f32_e32 v30, v28, v21
	v_fma_f32 v32, -v20, v30, v28
	v_fmac_f32_e32 v30, v32, v21
	v_fma_f32 v20, -v20, v30, v28
	v_div_fmas_f32 v20, v20, v21, v30
	v_div_fixup_f32 v2, v20, v2, 1.0
	v_pk_mul_f32 v[10:11], v[10:11], v[2:3] op_sel_hi:[1,0]
	v_pk_mul_f32 v[16:17], v[2:3], v[16:17] op_sel_hi:[0,1]
	v_pk_mul_f32 v[86:87], v[50:51], v[10:11]
	v_mov_b32_e32 v11, v8
	v_mov_b32_e32 v8, v25
	v_pk_mul_f32 v[8:9], v[2:3], v[8:9] op_sel_hi:[0,1]
	v_pk_mul_f32 v[98:99], v[38:39], v[16:17]
	v_mov_b32_e32 v17, v14
	v_mov_b32_e32 v14, v23
	v_pk_mul_f32 v[82:83], v[54:55], v[8:9]
	v_mov_b32_e32 v9, v6
	v_mov_b32_e32 v6, v35
	v_pk_mul_f32 v[18:19], v[2:3], v[18:19] op_sel_hi:[0,1]
	v_mov_b32_e32 v16, v22
	v_pk_mul_f32 v[14:15], v[2:3], v[14:15] op_sel_hi:[0,1]
	v_pk_mul_f32 v[12:13], v[2:3], v[12:13] op_sel_hi:[0,1]
	v_mov_b32_e32 v30, v29
	v_mov_b32_e32 v10, v24
	v_mov_b32_e32 v8, v34
	v_pk_mul_f32 v[6:7], v[2:3], v[6:7] op_sel_hi:[0,1]
	v_pk_mul_f32 v[4:5], v[2:3], v[4:5] op_sel_hi:[0,1]
	v_pk_mul_f32 v[96:97], v[36:37], v[18:19]
	v_pk_mul_f32 v[16:17], v[2:3], v[16:17] op_sel_hi:[0,1]
	v_pk_mul_f32 v[94:95], v[42:43], v[14:15]
	v_pk_mul_f32 v[14:15], v[2:3], v[26:27] op_sel_hi:[0,1]
	v_pk_mul_f32 v[90:91], v[46:47], v[12:13]
	v_pk_mul_f32 v[12:13], v[30:31], v[2:3] op_sel_hi:[1,0]
	v_pk_mul_f32 v[10:11], v[2:3], v[10:11] op_sel_hi:[0,1]
	v_pk_mul_f32 v[8:9], v[2:3], v[8:9] op_sel_hi:[0,1]
	v_pk_mul_f32 v[78:79], v[58:59], v[6:7]
	v_pk_mul_f32 v[6:7], v[2:3], v[70:71] op_sel_hi:[0,1]
	v_pk_mul_f32 v[74:75], v[62:63], v[4:5]
	v_pk_mul_f32 v[4:5], v[138:139], v[2:3] op_sel_hi:[1,0]
	v_pk_mul_f32 v[0:1], v[0:1], v[2:3] op_sel_hi:[1,0]
	v_pk_mul_f32 v[92:93], v[40:41], v[16:17]
	v_pk_mul_f32 v[88:89], v[44:45], v[14:15]
	v_pk_mul_f32 v[84:85], v[48:49], v[12:13]
	v_pk_mul_f32 v[80:81], v[52:53], v[10:11]
	v_pk_mul_f32 v[76:77], v[56:57], v[8:9]
	v_pk_mul_f32 v[72:73], v[60:61], v[6:7]
	v_pk_mul_f32 v[70:71], v[66:67], v[0:1]
	v_pk_mul_f32 v[68:69], v[64:65], v[4:5]
	ds_write_b128 v101, v[96:99]
	ds_write_b128 v101, v[92:95] offset:1152
	ds_write_b128 v101, v[88:91] offset:2304
	ds_write_b128 v101, v[84:87] offset:3456
	ds_write_b128 v101, v[80:83] offset:4608
	ds_write_b128 v101, v[76:79] offset:5760
	ds_write_b128 v101, v[72:75] offset:6912
	ds_write_b128 v101, v[68:71] offset:8064
	s_waitcnt lgkmcnt(0)
	ds_read_b128 v[20:23], v135 offset:64
	ds_read_b128 v[4:7], v135
	ds_read_b128 v[8:11], v135 offset:16
	ds_read_b128 v[12:15], v135 offset:32
	ds_read_b128 v[16:19], v135 offset:48
	ds_read_b128 v[24:27], v135 offset:80
	ds_read_b128 v[28:31], v135 offset:96
	ds_read_b128 v[32:35], v135 offset:112
	s_waitcnt lgkmcnt(7)
	v_max_f32_e64 v0, |v20|, |v20|
	s_waitcnt lgkmcnt(6)
	v_max_f32_e64 v1, |v4|, |v4|
	v_max_f32_e32 v0, v1, v0
	v_max_f32_e64 v1, |v21|, |v21|
	v_max_f32_e64 v2, |v5|, |v5|
	v_max_f32_e32 v1, v2, v1
	v_max3_f32 v0, v0, 0, v1
	v_max_f32_e64 v1, |v22|, |v22|
	v_max_f32_e64 v2, |v6|, |v6|
	v_max_f32_e32 v1, v2, v1
	v_max_f32_e64 v2, |v23|, |v23|
	v_max_f32_e64 v136, |v7|, |v7|
	v_max_f32_e32 v2, v136, v2
	v_max3_f32 v0, v0, v1, v2
	s_waitcnt lgkmcnt(2)
	v_max_f32_e64 v1, |v24|, |v24|
	v_max_f32_e64 v2, |v8|, |v8|
	v_max_f32_e32 v1, v2, v1
	v_max_f32_e64 v2, |v25|, |v25|
	v_max_f32_e64 v136, |v9|, |v9|
	v_max_f32_e32 v2, v136, v2
	v_max3_f32 v0, v0, v1, v2
	v_max_f32_e64 v1, |v26|, |v26|
	v_max_f32_e64 v2, |v10|, |v10|
	v_max_f32_e32 v1, v2, v1
	v_max_f32_e64 v2, |v27|, |v27|
	v_max_f32_e64 v136, |v11|, |v11|
	v_max_f32_e32 v2, v136, v2
	v_max3_f32 v0, v0, v1, v2
	s_waitcnt lgkmcnt(1)
	v_max_f32_e64 v1, |v28|, |v28|
	v_max_f32_e64 v2, |v12|, |v12|
	v_max_f32_e32 v1, v2, v1
	v_max_f32_e64 v2, |v29|, |v29|
	v_max_f32_e64 v136, |v13|, |v13|
	v_max_f32_e32 v2, v136, v2
	v_max3_f32 v0, v0, v1, v2
	v_max_f32_e64 v1, |v30|, |v30|
	v_max_f32_e64 v2, |v14|, |v14|
	v_max_f32_e32 v1, v2, v1
	v_max_f32_e64 v2, |v31|, |v31|
	v_max_f32_e64 v136, |v15|, |v15|
	v_max_f32_e32 v2, v136, v2
	v_max3_f32 v0, v0, v1, v2
	s_waitcnt lgkmcnt(0)
; #define LAS __attribute__((address_space(3)))
; __device__ __forceinline__ void mx6_block(const v16f& a, const v16f& b, float pre, u32x4& w0, u32x4& w1) {
;     float amax = 0.f;
; #pragma unroll
;     for (int i = 0; i < 16; ++i) amax = fmaxf(amax, fmaxf(__builtin_fabsf(a[i]), __builtin_fabsf(b[i])));
;     amax *= __builtin_fabsf(pre);
;     int eb = (int)((__float_as_uint(amax) >> 23) & 0xFFu) - 2; eb = eb < 1 ? 1 : eb;
;     const float mul = pre * __uint_as_float((unsigned)(254 - eb) << 23);
;     const v16f as = a * mul, bs = b * mul;
;     const auto r = __builtin_amdgcn_cvt_scalef32_2xpk16_fp6_f32(as, bs, 1.0f);
;     w0 = (u32x4){(unsigned)r[0], (unsigned)r[1], (unsigned)r[2], (unsigned)r[3]}; w1 = (u32x4){(unsigned)r[4], (unsigned)r[5], (unsigned)eb, 0u};
; __device__ __forceinline__ void phase_norm_route(const bf16_t* x, const float* g, const float* router, bf16_t* H, int* tok_info, unsigned* cnt, LAS unsigned char* lds, int tid, int wid, int lane) {
;     ...
;               u32x4 w0, w1; pg8::mx6_block(a, b, 1.0f, w0, w1);
;               unsigned char* q = h8 + (lane >> 2) * 128 + (lane & 3) * 16;
;               *(u32x4*)q = w0; *(u32x4*)(q + 64) = w1; }
;             float lg[8];
; #pragma unroll
;             for (int e = 0; e < 8; ++e) { float s = 0.f;
; #pragma unroll
;                 for (int j = 0; j < 8; ++j) { const f32x4 r = *(const LAS f32x4*)(RT + e * 2048 + 4 * lane + 256 * j); s += (v[j][0] * r[0] + v[j][1] * r[1]) + (v[j][2] * r[2] + v[j][3] * r[3]); }
	v_max_f32_e64 v1, |v32|, |v32|
	v_max_f32_e64 v2, |v16|, |v16|
	v_max_f32_e32 v1, v2, v1
	v_max_f32_e64 v2, |v33|, |v33|
	v_max_f32_e64 v136, |v17|, |v17|
	v_max_f32_e32 v2, v136, v2
	v_max3_f32 v0, v0, v1, v2
	v_max_f32_e64 v1, |v34|, |v34|
	v_max_f32_e64 v2, |v18|, |v18|
	v_max_f32_e32 v1, v2, v1
	v_max_f32_e64 v2, |v35|, |v35|
	v_max_f32_e64 v136, |v19|, |v19|
	v_max_f32_e32 v2, v136, v2
	v_max3_f32 v0, v0, v1, v2
	v_bfe_u32 v0, v0, 23, 8
	v_max_u32_e32 v0, 3, v0
	v_add_u32_e32 v2, -2, v0
	v_lshlrev_b32_e32 v0, 23, v0
	v_sub_u32_e32 v0, 0x80000000, v0
	v_pk_mul_f32 v[18:19], v[18:19], v[0:1] op_sel_hi:[1,0]
	v_pk_mul_f32 v[16:17], v[16:17], v[0:1] op_sel_hi:[1,0]
	v_pk_mul_f32 v[14:15], v[14:15], v[0:1] op_sel_hi:[1,0]
	v_pk_mul_f32 v[12:13], v[12:13], v[0:1] op_sel_hi:[1,0]
	v_pk_mul_f32 v[10:11], v[10:11], v[0:1] op_sel_hi:[1,0]
	v_pk_mul_f32 v[8:9], v[8:9], v[0:1] op_sel_hi:[1,0]
	v_pk_mul_f32 v[6:7], v[6:7], v[0:1] op_sel_hi:[1,0]
	v_pk_mul_f32 v[4:5], v[4:5], v[0:1] op_sel_hi:[1,0]
	v_pk_mul_f32 v[34:35], v[34:35], v[0:1] op_sel_hi:[1,0]
	v_pk_mul_f32 v[32:33], v[32:33], v[0:1] op_sel_hi:[1,0]
	v_pk_mul_f32 v[30:31], v[30:31], v[0:1] op_sel_hi:[1,0]
	v_pk_mul_f32 v[28:29], v[28:29], v[0:1] op_sel_hi:[1,0]
	v_pk_mul_f32 v[26:27], v[26:27], v[0:1] op_sel_hi:[1,0]
	v_pk_mul_f32 v[24:25], v[24:25], v[0:1] op_sel_hi:[1,0]
	v_pk_mul_f32 v[22:23], v[22:23], v[0:1] op_sel_hi:[1,0]
	v_pk_mul_f32 v[20:21], v[20:21], v[0:1] op_sel_hi:[1,0]
	s_waitcnt lgkmcnt(0)
	s_nop 0
	v_cvt_scalef32_2xpk16_fp6_f32 v[4:9], v[4:19], v[20:35], 1.0
	v_mov_b32_e32 v0, v8
	v_mov_b32_e32 v1, v9
	global_store_dwordx4 v[110:111], v[4:7], off
	global_store_dwordx4 v[110:111], v[0:3], off offset:64
	ds_read_b128 v[20:23], v133
	ds_read_b128 v[24:27], v133 offset:1024
	ds_read_b128 v[28:31], v133 offset:2048
	ds_read_b128 v[32:35], v133 offset:3072
	ds_read_b128 v[16:19], v133 offset:4096
	ds_read_b128 v[12:15], v133 offset:5120
	ds_read_b128 v[8:11], v133 offset:6144
	ds_read_b128 v[4:7], v133 offset:7168
	ds_read_b128 v[136:139], v133 offset:8192
	ds_read_b128 v[140:143], v133 offset:9216
	s_waitcnt lgkmcnt(9)
	v_mov_b32_e32 v1, v21
	s_waitcnt lgkmcnt(1)
	v_mov_b32_e32 v0, v136
	v_pk_mul_f32 v[0:1], v[96:97], v[0:1]
	v_pk_mov_b32 v[20:21], v[136:137], v[20:21] op_sel:[1,0]
	s_nop 0
	v_pk_fma_f32 v[0:1], v[96:97], v[20:21], v[0:1] op_sel:[1,0,0] op_sel_hi:[0,1,1]
	v_mov_b32_e32 v20, v138
	v_mov_b32_e32 v21, v23
	v_pk_mul_f32 v[20:21], v[98:99], v[20:21]
	v_pk_mov_b32 v[22:23], v[138:139], v[22:23] op_sel:[1,0]
	s_nop 0
	v_pk_fma_f32 v[20:21], v[98:99], v[22:23], v[20:21] op_sel:[1,0,0] op_sel_hi:[0,1,1]
	v_pk_add_f32 v[0:1], v[0:1], v[20:21]
	s_waitcnt lgkmcnt(0)
	v_mov_b32_e32 v20, v140
	v_mov_b32_e32 v21, v25
	v_pk_mul_f32 v[20:21], v[92:93], v[20:21]
	v_pk_mov_b32 v[22:23], v[140:141], v[24:25] op_sel:[1,0]
	v_pk_mov_b32 v[24:25], v[142:143], v[26:27] op_sel:[1,0]
	v_pk_fma_f32 v[20:21], v[92:93], v[22:23], v[20:21] op_sel:[1,0,0] op_sel_hi:[0,1,1]
	v_mov_b32_e32 v22, v142
	v_mov_b32_e32 v23, v27
	v_pk_mul_f32 v[22:23], v[94:95], v[22:23]
	v_pk_add_f32 v[0:1], v[0:1], 0 op_sel_hi:[1,0]
	v_pk_fma_f32 v[22:23], v[94:95], v[24:25], v[22:23] op_sel:[1,0,0] op_sel_hi:[0,1,1]
	v_pk_add_f32 v[20:21], v[20:21], v[22:23]
	v_mov_b32_e32 v25, v29
	v_pk_add_f32 v[0:1], v[0:1], v[20:21]
	ds_read_b128 v[20:23], v133 offset:10240
	s_waitcnt lgkmcnt(0)
	v_mov_b32_e32 v24, v20
	v_pk_mul_f32 v[24:25], v[88:89], v[24:25]
	v_pk_mov_b32 v[20:21], v[20:21], v[28:29] op_sel:[1,0]
	s_nop 0
	v_pk_fma_f32 v[20:21], v[88:89], v[20:21], v[24:25] op_sel:[1,0,0] op_sel_hi:[0,1,1]
	v_mov_b32_e32 v24, v22
	v_mov_b32_e32 v25, v31
	v_pk_mul_f32 v[24:25], v[90:91], v[24:25]
	v_pk_mov_b32 v[22:23], v[22:23], v[30:31] op_sel:[1,0]
	s_nop 0
	v_pk_fma_f32 v[22:23], v[90:91], v[22:23], v[24:25] op_sel:[1,0,0] op_sel_hi:[0,1,1]
	v_pk_add_f32 v[136:137], v[20:21], v[22:23]
	ds_read_b128 v[20:23], v133 offset:11264
	v_mov_b32_e32 v25, v33
	v_pk_add_f32 v[0:1], v[0:1], v[136:137]
	s_waitcnt lgkmcnt(0)
	v_mov_b32_e32 v24, v20
	v_pk_mul_f32 v[24:25], v[84:85], v[24:25]
	v_pk_mov_b32 v[20:21], v[20:21], v[32:33] op_sel:[1,0]
	s_nop 0
	v_pk_fma_f32 v[138:139], v[84:85], v[20:21], v[24:25] op_sel:[1,0,0] op_sel_hi:[0,1,1]
	v_mov_b32_e32 v20, v22
	v_mov_b32_e32 v21, v35
	v_pk_mul_f32 v[20:21], v[86:87], v[20:21]
	v_pk_mov_b32 v[22:23], v[22:23], v[34:35] op_sel:[1,0]
	v_mov_b32_e32 v25, v17
	v_pk_fma_f32 v[140:141], v[86:87], v[22:23], v[20:21] op_sel:[1,0,0] op_sel_hi:[0,1,1]
	ds_read_b128 v[20:23], v133 offset:12288
	v_pk_add_f32 v[136:137], v[138:139], v[140:141]
	s_waitcnt lgkmcnt(0)
	v_mov_b32_e32 v24, v20
	v_pk_mul_f32 v[142:143], v[80:81], v[24:25]
	v_mov_b32_e32 v24, v22
	v_mov_b32_e32 v25, v19
	v_pk_mul_f32 v[144:145], v[82:83], v[24:25]
	ds_read_b128 v[24:27], v133 offset:13312
	ds_read_b128 v[28:31], v133 offset:14336
	ds_read_b128 v[32:35], v133 offset:15360
	v_pk_mov_b32 v[16:17], v[20:21], v[16:17] op_sel:[1,0]
	v_pk_mov_b32 v[18:19], v[22:23], v[18:19] op_sel:[1,0]
	v_pk_fma_f32 v[16:17], v[80:81], v[16:17], v[142:143] op_sel:[1,0,0] op_sel_hi:[0,1,1]
	v_pk_fma_f32 v[18:19], v[82:83], v[18:19], v[144:145] op_sel:[1,0,0] op_sel_hi:[0,1,1]
	v_pk_add_f32 v[0:1], v[0:1], v[136:137]
	v_pk_add_f32 v[16:17], v[16:17], v[18:19]
	s_nop 0
	v_pk_add_f32 v[0:1], v[0:1], v[16:17]
	s_waitcnt lgkmcnt(2)
	v_mov_b32_e32 v16, v24
	v_mov_b32_e32 v17, v13
	v_pk_mul_f32 v[16:17], v[76:77], v[16:17]
	v_pk_mov_b32 v[12:13], v[24:25], v[12:13] op_sel:[1,0]
	s_nop 0
	v_pk_fma_f32 v[12:13], v[76:77], v[12:13], v[16:17] op_sel:[1,0,0] op_sel_hi:[0,1,1]
	v_mov_b32_e32 v16, v26
	v_mov_b32_e32 v17, v15
	v_pk_mul_f32 v[16:17], v[78:79], v[16:17]
	v_pk_mov_b32 v[14:15], v[26:27], v[14:15] op_sel:[1,0]
	s_nop 0
	v_pk_fma_f32 v[14:15], v[78:79], v[14:15], v[16:17] op_sel:[1,0,0] op_sel_hi:[0,1,1]
	v_pk_add_f32 v[12:13], v[12:13], v[14:15]
	s_nop 0
	v_pk_add_f32 v[0:1], v[0:1], v[12:13]
	s_waitcnt lgkmcnt(1)
; #define LAS __attribute__((address_space(3)))
; __device__ __forceinline__ void phase_norm_route(const bf16_t* x, const float* g, const float* router, bf16_t* H, int* tok_info, unsigned* cnt, LAS unsigned char* lds, int tid, int wid, int lane) {
;     ...
;             float lg[8];
; #pragma unroll
;             for (int e = 0; e < 8; ++e) { float s = 0.f;
; #pragma unroll
;                 for (int j = 0; j < 8; ++j) { const f32x4 r = *(const LAS f32x4*)(RT + e * 2048 + 4 * lane + 256 * j); s += (v[j][0] * r[0] + v[j][1] * r[1]) + (v[j][2] * r[2] + v[j][3] * r[3]); }
;                 lg[e] = wave_sum(s); }
	v_mov_b32_e32 v12, v28
	v_mov_b32_e32 v13, v9
	v_pk_mul_f32 v[12:13], v[72:73], v[12:13]
	v_pk_mov_b32 v[8:9], v[28:29], v[8:9] op_sel:[1,0]
	s_nop 0
	v_pk_fma_f32 v[8:9], v[72:73], v[8:9], v[12:13] op_sel:[1,0,0] op_sel_hi:[0,1,1]
	v_mov_b32_e32 v12, v30
	v_mov_b32_e32 v13, v11
	v_pk_mul_f32 v[12:13], v[74:75], v[12:13]
	v_pk_mov_b32 v[10:11], v[30:31], v[10:11] op_sel:[1,0]
	s_nop 0
	v_pk_fma_f32 v[10:11], v[74:75], v[10:11], v[12:13] op_sel:[1,0,0] op_sel_hi:[0,1,1]
	v_pk_add_f32 v[8:9], v[8:9], v[10:11]
	s_nop 0
	v_pk_add_f32 v[0:1], v[0:1], v[8:9]
	s_waitcnt lgkmcnt(0)
	v_mov_b32_e32 v8, v32
	v_mov_b32_e32 v9, v5
	v_pk_mul_f32 v[8:9], v[68:69], v[8:9]
	v_pk_mov_b32 v[4:5], v[32:33], v[4:5] op_sel:[1,0]
	s_nop 0
	v_pk_fma_f32 v[4:5], v[68:69], v[4:5], v[8:9] op_sel:[1,0,0] op_sel_hi:[0,1,1]
	v_mov_b32_e32 v8, v34
	v_mov_b32_e32 v9, v7
	v_pk_mul_f32 v[8:9], v[70:71], v[8:9]
	v_pk_mov_b32 v[6:7], v[34:35], v[6:7] op_sel:[1,0]
	s_nop 0
	v_pk_fma_f32 v[6:7], v[70:71], v[6:7], v[8:9] op_sel:[1,0,0] op_sel_hi:[0,1,1]
	v_pk_add_f32 v[4:5], v[4:5], v[6:7]
	ds_read_b128 v[208:211], v133 offset:16384
	ds_read_b128 v[212:215], v133 offset:17408
	ds_read_b128 v[216:219], v133 offset:18432
	ds_read_b128 v[220:223], v133 offset:19456
	ds_read_b128 v[224:227], v133 offset:20480
	v_pk_add_f32 v[0:1], v[0:1], v[4:5]
	s_nop 1
	v_add_f32_dpp v0, v0, v0 quad_perm:[1,0,3,2] row_mask:0xf bank_mask:0xf
	s_nop 1
	v_add_f32_dpp v0, v0, v0 quad_perm:[2,3,0,1] row_mask:0xf bank_mask:0xf
	s_nop 1
	v_add_f32_dpp v0, v0, v0 row_half_mirror row_mask:0xf bank_mask:0xf
	s_nop 1
	v_add_f32_dpp v0, v0, v0 row_mirror row_mask:0xf bank_mask:0xf
	v_mov_b32_e32 v4, v0
	s_nop 1
	v_permlane16_swap_b32_e32 v4, v0
	v_add_f32_e32 v0, v0, v4
	v_mov_b32_e32 v4, v0
	s_nop 1
	v_permlane32_swap_b32_e32 v4, v0
	v_add_f32_e32 v0, v0, v4
	s_nop 1
	v_add_f32_dpp v1, v1, v1 quad_perm:[1,0,3,2] row_mask:0xf bank_mask:0xf
	s_nop 1
	v_add_f32_dpp v1, v1, v1 quad_perm:[2,3,0,1] row_mask:0xf bank_mask:0xf
	s_nop 1
	v_add_f32_dpp v1, v1, v1 row_half_mirror row_mask:0xf bank_mask:0xf
	s_nop 1
	v_add_f32_dpp v1, v1, v1 row_mirror row_mask:0xf bank_mask:0xf
	v_mov_b32_e32 v5, v1
	s_nop 1
	v_permlane16_swap_b32_e32 v5, v1
	v_add_f32_e32 v1, v1, v5
	v_mov_b32_e32 v5, v1
	s_nop 1
	v_permlane32_swap_b32_e32 v5, v1
	v_add_f32_e32 v1, v1, v5
	s_nop 0
	s_waitcnt lgkmcnt(4)
	v_mul_f32_e32 v2, v97, v209
	v_fmac_f32_e32 v2, v96, v208
	v_mul_f32_e32 v6, v99, v211
	v_fmac_f32_e32 v6, v98, v210
	v_add_f32_e32 v2, v2, v6
	ds_read_b128 v[228:231], v133 offset:21504
	v_add_f32_e32 v2, 0, v2
	s_waitcnt lgkmcnt(5)
	s_nop 0
	s_nop 0
	s_nop 0
	s_waitcnt lgkmcnt(4)
	v_mul_f32_e32 v7, v93, v213
	v_fmac_f32_e32 v7, v92, v212
	v_mul_f32_e32 v6, v95, v215
	v_fmac_f32_e32 v6, v94, v214
	v_add_f32_e32 v6, v7, v6
	v_add_f32_e32 v2, v2, v6
	ds_read_b128 v[208:211], v133 offset:22528
	s_waitcnt lgkmcnt(5)
	s_nop 0
	s_nop 0
	s_nop 0
	s_waitcnt lgkmcnt(4)
	v_mul_f32_e32 v7, v89, v217
	v_fmac_f32_e32 v7, v88, v216
	v_mul_f32_e32 v6, v91, v219
	v_fmac_f32_e32 v6, v90, v218
	v_add_f32_e32 v6, v7, v6
	v_add_f32_e32 v2, v2, v6
	ds_read_b128 v[212:215], v133 offset:23552
	s_waitcnt lgkmcnt(5)
	s_nop 0
	s_nop 0
	s_nop 0
	s_waitcnt lgkmcnt(4)
	v_mul_f32_e32 v7, v85, v221
	v_fmac_f32_e32 v7, v84, v220
	v_mul_f32_e32 v6, v87, v223
	v_fmac_f32_e32 v6, v86, v222
	v_add_f32_e32 v6, v7, v6
	v_add_f32_e32 v2, v2, v6
	ds_read_b128 v[216:219], v133 offset:24576
	s_waitcnt lgkmcnt(5)
	s_nop 0
	s_nop 0
	s_nop 0
	s_waitcnt lgkmcnt(4)
	v_mul_f32_e32 v7, v81, v225
	v_fmac_f32_e32 v7, v80, v224
	v_mul_f32_e32 v6, v83, v227
	v_fmac_f32_e32 v6, v82, v226
	v_add_f32_e32 v6, v7, v6
	v_add_f32_e32 v2, v2, v6
	ds_read_b128 v[220:223], v133 offset:25600
	s_waitcnt lgkmcnt(5)
	s_nop 0
	s_nop 0
	s_nop 0
	s_waitcnt lgkmcnt(4)
	v_mul_f32_e32 v7, v77, v229
	v_fmac_f32_e32 v7, v76, v228
	v_mul_f32_e32 v6, v79, v231
	v_fmac_f32_e32 v6, v78, v230
	v_add_f32_e32 v6, v7, v6
	v_add_f32_e32 v2, v2, v6
	ds_read_b128 v[224:227], v133 offset:26624
	s_waitcnt lgkmcnt(4)
	v_mul_f32_e32 v7, v73, v209
	v_fmac_f32_e32 v7, v72, v208
	v_mul_f32_e32 v6, v75, v211
	v_fmac_f32_e32 v6, v74, v210
	v_add_f32_e32 v6, v7, v6
	v_add_f32_e32 v2, v2, v6
	ds_read_b128 v[228:231], v133 offset:27648
	s_waitcnt lgkmcnt(4)
	v_mul_f32_e32 v7, v69, v213
	v_fmac_f32_e32 v7, v68, v212
	v_mul_f32_e32 v6, v71, v215
	v_fmac_f32_e32 v6, v70, v214
	ds_read_b128 v[208:211], v133 offset:28672
	v_add_f32_e32 v6, v7, v6
	v_add_f32_e32 v2, v2, v6
	s_nop 1
	v_add_f32_dpp v2, v2, v2 quad_perm:[1,0,3,2] row_mask:0xf bank_mask:0xf
	s_nop 1
	v_add_f32_dpp v2, v2, v2 quad_perm:[2,3,0,1] row_mask:0xf bank_mask:0xf
	s_nop 1
	v_add_f32_dpp v2, v2, v2 row_half_mirror row_mask:0xf bank_mask:0xf
	s_nop 1
	v_add_f32_dpp v2, v2, v2 row_mirror row_mask:0xf bank_mask:0xf
	v_mov_b32_e32 v6, v2
	s_nop 1
	v_permlane16_swap_b32_e32 v6, v2
	v_add_f32_e32 v2, v2, v6
	v_mov_b32_e32 v6, v2
	s_nop 1
	v_permlane32_swap_b32_e32 v6, v2
	v_add_f32_e32 v2, v2, v6
	s_waitcnt lgkmcnt(4)
	v_mul_f32_e32 v7, v97, v217
	v_fmac_f32_e32 v7, v96, v216
	v_mul_f32_e32 v8, v99, v219
	v_fmac_f32_e32 v8, v98, v218
	v_add_f32_e32 v7, v7, v8
	ds_read_b128 v[212:215], v133 offset:29696
	v_add_f32_e32 v7, 0, v7
	s_waitcnt lgkmcnt(5)
	s_nop 0
	s_nop 0
	s_waitcnt lgkmcnt(4)
	v_mul_f32_e32 v9, v93, v221
	v_fmac_f32_e32 v9, v92, v220
	v_mul_f32_e32 v8, v95, v223
	v_fmac_f32_e32 v8, v94, v222
	v_add_f32_e32 v8, v9, v8
	v_add_f32_e32 v7, v7, v8
	ds_read_b128 v[216:219], v133 offset:30720
	s_waitcnt lgkmcnt(5)
	s_nop 0
	s_nop 0
	s_waitcnt lgkmcnt(4)
; #define LAS __attribute__((address_space(3)))
; __device__ __forceinline__ void phase_norm_route(const bf16_t* x, const float* g, const float* router, bf16_t* H, int* tok_info, unsigned* cnt, LAS unsigned char* lds, int tid, int wid, int lane) {
;     ...
;             float lg[8];
; #pragma unroll
;             for (int e = 0; e < 8; ++e) { float s = 0.f;
; #pragma unroll
;                 for (int j = 0; j < 8; ++j) { const f32x4 r = *(const LAS f32x4*)(RT + e * 2048 + 4 * lane + 256 * j); s += (v[j][0] * r[0] + v[j][1] * r[1]) + (v[j][2] * r[2] + v[j][3] * r[3]); }
;                 lg[e] = wave_sum(s); }
	v_mul_f32_e32 v9, v89, v225
	v_fmac_f32_e32 v9, v88, v224
	v_mul_f32_e32 v8, v91, v227
	v_fmac_f32_e32 v8, v90, v226
	v_add_f32_e32 v8, v9, v8
	v_add_f32_e32 v7, v7, v8
	ds_read_b128 v[220:223], v133 offset:31744
	s_waitcnt lgkmcnt(5)
	s_nop 0
	s_nop 0
	s_waitcnt lgkmcnt(4)
	v_mul_f32_e32 v9, v85, v229
	v_fmac_f32_e32 v9, v84, v228
	v_mul_f32_e32 v8, v87, v231
	v_fmac_f32_e32 v8, v86, v230
	v_add_f32_e32 v8, v9, v8
	v_add_f32_e32 v7, v7, v8
	ds_read_b128 v[224:227], v133 offset:32768
	s_waitcnt lgkmcnt(5)
	s_nop 0
	s_nop 0
	s_waitcnt lgkmcnt(4)
	v_mul_f32_e32 v9, v81, v209
	v_fmac_f32_e32 v9, v80, v208
	v_mul_f32_e32 v8, v83, v211
	v_fmac_f32_e32 v8, v82, v210
	v_add_f32_e32 v8, v9, v8
	v_add_f32_e32 v7, v7, v8
	ds_read_b128 v[228:231], v133 offset:33792
	s_waitcnt lgkmcnt(5)
	s_nop 0
	s_nop 0
	s_waitcnt lgkmcnt(4)
	v_mul_f32_e32 v9, v77, v213
	v_fmac_f32_e32 v9, v76, v212
	v_mul_f32_e32 v8, v79, v215
	v_fmac_f32_e32 v8, v78, v214
	v_add_f32_e32 v8, v9, v8
	v_add_f32_e32 v7, v7, v8
	ds_read_b128 v[208:211], v133 offset:34816
	s_waitcnt lgkmcnt(4)
	v_mul_f32_e32 v9, v73, v217
	v_fmac_f32_e32 v9, v72, v216
	v_mul_f32_e32 v8, v75, v219
	v_fmac_f32_e32 v8, v74, v218
	v_add_f32_e32 v8, v9, v8
	v_add_f32_e32 v7, v7, v8
	ds_read_b128 v[212:215], v133 offset:35840
	s_waitcnt lgkmcnt(4)
	v_mul_f32_e32 v9, v69, v221
	v_fmac_f32_e32 v9, v68, v220
	v_mul_f32_e32 v8, v71, v223
	v_fmac_f32_e32 v8, v70, v222
	ds_read_b128 v[216:219], v133 offset:36864
	v_add_f32_e32 v8, v9, v8
	v_add_f32_e32 v7, v7, v8
	s_nop 1
	v_add_f32_dpp v7, v7, v7 quad_perm:[1,0,3,2] row_mask:0xf bank_mask:0xf
	s_nop 1
	v_add_f32_dpp v7, v7, v7 quad_perm:[2,3,0,1] row_mask:0xf bank_mask:0xf
	s_nop 1
	v_add_f32_dpp v7, v7, v7 row_half_mirror row_mask:0xf bank_mask:0xf
	s_nop 1
	v_add_f32_dpp v7, v7, v7 row_mirror row_mask:0xf bank_mask:0xf
	v_mov_b32_e32 v8, v7
	s_nop 1
	v_permlane16_swap_b32_e32 v8, v7
	v_add_f32_e32 v7, v7, v8
	v_mov_b32_e32 v8, v7
	s_nop 1
	v_permlane32_swap_b32_e32 v8, v7
	v_add_f32_e32 v7, v7, v8
	s_waitcnt lgkmcnt(4)
	v_mul_f32_e32 v9, v97, v225
	v_fmac_f32_e32 v9, v96, v224
	v_mul_f32_e32 v10, v99, v227
	v_fmac_f32_e32 v10, v98, v226
	v_add_f32_e32 v9, v9, v10
	ds_read_b128 v[220:223], v133 offset:37888
	v_add_f32_e32 v9, 0, v9
	s_waitcnt lgkmcnt(5)
	s_nop 0
	s_nop 0
	s_waitcnt lgkmcnt(4)
	v_mul_f32_e32 v11, v93, v229
	v_fmac_f32_e32 v11, v92, v228
	v_mul_f32_e32 v10, v95, v231
	v_fmac_f32_e32 v10, v94, v230
	v_add_f32_e32 v10, v11, v10
	v_add_f32_e32 v9, v9, v10
	ds_read_b128 v[224:227], v133 offset:38912
	s_waitcnt lgkmcnt(5)
	s_nop 0
	s_nop 0
	s_waitcnt lgkmcnt(4)
	v_mul_f32_e32 v11, v89, v209
	v_fmac_f32_e32 v11, v88, v208
	v_mul_f32_e32 v10, v91, v211
	v_fmac_f32_e32 v10, v90, v210
	v_add_f32_e32 v10, v11, v10
	v_add_f32_e32 v9, v9, v10
	ds_read_b128 v[228:231], v133 offset:39936
	s_waitcnt lgkmcnt(5)
	s_nop 0
	s_nop 0
	s_waitcnt lgkmcnt(4)
	v_mul_f32_e32 v11, v85, v213
	v_fmac_f32_e32 v11, v84, v212
	v_mul_f32_e32 v10, v87, v215
	v_fmac_f32_e32 v10, v86, v214
	v_add_f32_e32 v10, v11, v10
	v_add_f32_e32 v9, v9, v10
	ds_read_b128 v[208:211], v133 offset:40960
	s_waitcnt lgkmcnt(5)
	s_nop 0
	s_nop 0
	s_waitcnt lgkmcnt(4)
	v_mul_f32_e32 v11, v81, v217
	v_fmac_f32_e32 v11, v80, v216
	v_mul_f32_e32 v10, v83, v219
	v_fmac_f32_e32 v10, v82, v218
	v_add_f32_e32 v10, v11, v10
	v_add_f32_e32 v9, v9, v10
	ds_read_b128 v[212:215], v133 offset:41984
	s_waitcnt lgkmcnt(5)
	s_nop 0
	s_nop 0
	s_waitcnt lgkmcnt(4)
	v_mul_f32_e32 v11, v77, v221
	v_fmac_f32_e32 v11, v76, v220
	v_mul_f32_e32 v10, v79, v223
	v_fmac_f32_e32 v10, v78, v222
	v_add_f32_e32 v10, v11, v10
	v_add_f32_e32 v9, v9, v10
	ds_read_b128 v[216:219], v133 offset:43008
	s_waitcnt lgkmcnt(4)
	v_mul_f32_e32 v11, v73, v225
	v_fmac_f32_e32 v11, v72, v224
	v_mul_f32_e32 v10, v75, v227
	v_fmac_f32_e32 v10, v74, v226
	v_add_f32_e32 v10, v11, v10
	v_add_f32_e32 v9, v9, v10
	ds_read_b128 v[220:223], v133 offset:44032
	s_waitcnt lgkmcnt(4)
	v_mul_f32_e32 v11, v69, v229
	v_fmac_f32_e32 v11, v68, v228
	v_mul_f32_e32 v10, v71, v231
	v_fmac_f32_e32 v10, v70, v230
	ds_read_b128 v[224:227], v133 offset:45056
	v_add_f32_e32 v10, v11, v10
	v_add_f32_e32 v9, v9, v10
	s_nop 1
	v_add_f32_dpp v9, v9, v9 quad_perm:[1,0,3,2] row_mask:0xf bank_mask:0xf
	s_nop 1
	v_add_f32_dpp v9, v9, v9 quad_perm:[2,3,0,1] row_mask:0xf bank_mask:0xf
	s_nop 1
	v_add_f32_dpp v9, v9, v9 row_half_mirror row_mask:0xf bank_mask:0xf
	s_nop 1
	v_add_f32_dpp v9, v9, v9 row_mirror row_mask:0xf bank_mask:0xf
	v_mov_b32_e32 v10, v9
	s_nop 1
	v_permlane16_swap_b32_e32 v10, v9
	v_add_f32_e32 v9, v9, v10
	v_mov_b32_e32 v10, v9
	s_nop 1
	v_permlane32_swap_b32_e32 v10, v9
	v_add_f32_e32 v9, v9, v10
	s_waitcnt lgkmcnt(4)
	v_mul_f32_e32 v11, v97, v209
	v_fmac_f32_e32 v11, v96, v208
	v_mul_f32_e32 v12, v99, v211
	v_fmac_f32_e32 v12, v98, v210
	v_add_f32_e32 v11, v11, v12
	ds_read_b128 v[228:231], v133 offset:46080
	v_add_f32_e32 v11, 0, v11
	s_waitcnt lgkmcnt(5)
	s_nop 0
	s_nop 0
	s_waitcnt lgkmcnt(4)
	v_mul_f32_e32 v13, v93, v213
	v_fmac_f32_e32 v13, v92, v212
	v_mul_f32_e32 v12, v95, v215
	v_fmac_f32_e32 v12, v94, v214
	v_add_f32_e32 v12, v13, v12
	v_add_f32_e32 v11, v11, v12
	ds_read_b128 v[208:211], v133 offset:47104
	s_waitcnt lgkmcnt(5)
	s_nop 0
	s_nop 0
	s_waitcnt lgkmcnt(4)
	v_mul_f32_e32 v13, v89, v217
	v_fmac_f32_e32 v13, v88, v216
	v_mul_f32_e32 v12, v91, v219
	v_fmac_f32_e32 v12, v90, v218
	v_add_f32_e32 v12, v13, v12
	v_add_f32_e32 v11, v11, v12
	ds_read_b128 v[212:215], v133 offset:48128
	s_waitcnt lgkmcnt(5)
	s_nop 0
	s_nop 0
	s_waitcnt lgkmcnt(4)
; #define LAS __attribute__((address_space(3)))
; __device__ __forceinline__ void phase_norm_route(const bf16_t* x, const float* g, const float* router, bf16_t* H, int* tok_info, unsigned* cnt, LAS unsigned char* lds, int tid, int wid, int lane) {
;     ...
;             float lg[8];
; #pragma unroll
;             for (int e = 0; e < 8; ++e) { float s = 0.f;
; #pragma unroll
;                 for (int j = 0; j < 8; ++j) { const f32x4 r = *(const LAS f32x4*)(RT + e * 2048 + 4 * lane + 256 * j); s += (v[j][0] * r[0] + v[j][1] * r[1]) + (v[j][2] * r[2] + v[j][3] * r[3]); }
;                 lg[e] = wave_sum(s); }
	v_mul_f32_e32 v13, v85, v221
	v_fmac_f32_e32 v13, v84, v220
	v_mul_f32_e32 v12, v87, v223
	v_fmac_f32_e32 v12, v86, v222
	v_add_f32_e32 v12, v13, v12
	v_add_f32_e32 v11, v11, v12
	ds_read_b128 v[216:219], v133 offset:49152
	s_waitcnt lgkmcnt(5)
	s_nop 0
	s_nop 0
	s_waitcnt lgkmcnt(4)
	v_mul_f32_e32 v13, v81, v225
	v_fmac_f32_e32 v13, v80, v224
	v_mul_f32_e32 v12, v83, v227
	v_fmac_f32_e32 v12, v82, v226
	v_add_f32_e32 v12, v13, v12
	v_add_f32_e32 v11, v11, v12
	ds_read_b128 v[220:223], v133 offset:50176
	s_waitcnt lgkmcnt(5)
	s_nop 0
	s_nop 0
	s_waitcnt lgkmcnt(4)
	v_mul_f32_e32 v13, v77, v229
	v_fmac_f32_e32 v13, v76, v228
	v_mul_f32_e32 v12, v79, v231
	v_fmac_f32_e32 v12, v78, v230
	v_add_f32_e32 v12, v13, v12
	v_add_f32_e32 v11, v11, v12
	ds_read_b128 v[224:227], v133 offset:51200
	s_waitcnt lgkmcnt(4)
	v_mul_f32_e32 v13, v73, v209
	v_fmac_f32_e32 v13, v72, v208
	v_mul_f32_e32 v12, v75, v211
	v_fmac_f32_e32 v12, v74, v210
	v_add_f32_e32 v12, v13, v12
	v_add_f32_e32 v11, v11, v12
	ds_read_b128 v[228:231], v133 offset:52224
	s_waitcnt lgkmcnt(4)
	v_mul_f32_e32 v13, v69, v213
	v_fmac_f32_e32 v13, v68, v212
	v_mul_f32_e32 v12, v71, v215
	v_fmac_f32_e32 v12, v70, v214
	ds_read_b128 v[208:211], v133 offset:53248
	v_add_f32_e32 v12, v13, v12
	v_add_f32_e32 v11, v11, v12
	s_nop 1
	v_add_f32_dpp v11, v11, v11 quad_perm:[1,0,3,2] row_mask:0xf bank_mask:0xf
	s_nop 1
	v_add_f32_dpp v11, v11, v11 quad_perm:[2,3,0,1] row_mask:0xf bank_mask:0xf
	s_nop 1
	v_add_f32_dpp v11, v11, v11 row_half_mirror row_mask:0xf bank_mask:0xf
	s_nop 1
	v_add_f32_dpp v11, v11, v11 row_mirror row_mask:0xf bank_mask:0xf
	v_mov_b32_e32 v12, v11
	s_nop 1
	v_permlane16_swap_b32_e32 v12, v11
	v_add_f32_e32 v11, v11, v12
	v_mov_b32_e32 v12, v11
	s_nop 1
	v_permlane32_swap_b32_e32 v12, v11
	v_add_f32_e32 v11, v11, v12
	s_waitcnt lgkmcnt(4)
	v_mul_f32_e32 v13, v97, v217
	v_fmac_f32_e32 v13, v96, v216
	v_mul_f32_e32 v14, v99, v219
	v_fmac_f32_e32 v14, v98, v218
	v_add_f32_e32 v13, v13, v14
	ds_read_b128 v[212:215], v133 offset:54272
	v_add_f32_e32 v13, 0, v13
	s_waitcnt lgkmcnt(5)
	s_nop 0
	s_nop 0
	s_waitcnt lgkmcnt(4)
	v_mul_f32_e32 v15, v93, v221
	v_fmac_f32_e32 v15, v92, v220
	v_mul_f32_e32 v14, v95, v223
	v_fmac_f32_e32 v14, v94, v222
	v_add_f32_e32 v14, v15, v14
	v_add_f32_e32 v13, v13, v14
	ds_read_b128 v[216:219], v133 offset:55296
	s_waitcnt lgkmcnt(5)
	s_nop 0
	s_nop 0
	s_waitcnt lgkmcnt(4)
	v_mul_f32_e32 v15, v89, v225
	v_fmac_f32_e32 v15, v88, v224
	v_mul_f32_e32 v14, v91, v227
	v_fmac_f32_e32 v14, v90, v226
	v_add_f32_e32 v14, v15, v14
	v_add_f32_e32 v13, v13, v14
	ds_read_b128 v[220:223], v133 offset:56320
	s_waitcnt lgkmcnt(5)
	s_nop 0
	s_nop 0
	s_waitcnt lgkmcnt(4)
	v_mul_f32_e32 v15, v85, v229
	v_fmac_f32_e32 v15, v84, v228
	v_mul_f32_e32 v14, v87, v231
	v_fmac_f32_e32 v14, v86, v230
	v_add_f32_e32 v14, v15, v14
	v_add_f32_e32 v13, v13, v14
	ds_read_b128 v[224:227], v133 offset:57344
	s_waitcnt lgkmcnt(5)
	s_nop 0
	s_nop 0
	s_waitcnt lgkmcnt(4)
	v_mul_f32_e32 v15, v81, v209
	v_fmac_f32_e32 v15, v80, v208
	v_mul_f32_e32 v14, v83, v211
	v_fmac_f32_e32 v14, v82, v210
	v_add_f32_e32 v14, v15, v14
	v_add_f32_e32 v13, v13, v14
	ds_read_b128 v[228:231], v133 offset:58368
	s_waitcnt lgkmcnt(5)
	s_nop 0
	s_nop 0
	s_waitcnt lgkmcnt(4)
	v_mul_f32_e32 v15, v77, v213
	v_fmac_f32_e32 v15, v76, v212
	v_mul_f32_e32 v14, v79, v215
	v_fmac_f32_e32 v14, v78, v214
	v_add_f32_e32 v14, v15, v14
	v_add_f32_e32 v13, v13, v14
	ds_read_b128 v[208:211], v133 offset:59392
	s_waitcnt lgkmcnt(4)
	v_mul_f32_e32 v15, v73, v217
	v_fmac_f32_e32 v15, v72, v216
	v_mul_f32_e32 v14, v75, v219
	v_fmac_f32_e32 v14, v74, v218
	v_add_f32_e32 v14, v15, v14
	v_add_f32_e32 v13, v13, v14
	ds_read_b128 v[212:215], v133 offset:60416
	s_waitcnt lgkmcnt(4)
	v_mul_f32_e32 v15, v69, v221
	v_fmac_f32_e32 v15, v68, v220
	v_mul_f32_e32 v14, v71, v223
	v_fmac_f32_e32 v14, v70, v222
	ds_read_b128 v[216:219], v133 offset:61440
	v_add_f32_e32 v14, v15, v14
	v_add_f32_e32 v13, v13, v14
	s_nop 1
	v_add_f32_dpp v13, v13, v13 quad_perm:[1,0,3,2] row_mask:0xf bank_mask:0xf
	s_nop 1
	v_add_f32_dpp v13, v13, v13 quad_perm:[2,3,0,1] row_mask:0xf bank_mask:0xf
	s_nop 1
	v_add_f32_dpp v13, v13, v13 row_half_mirror row_mask:0xf bank_mask:0xf
	s_nop 1
	v_add_f32_dpp v13, v13, v13 row_mirror row_mask:0xf bank_mask:0xf
	v_mov_b32_e32 v14, v13
	s_nop 1
	v_permlane16_swap_b32_e32 v14, v13
	v_add_f32_e32 v13, v13, v14
	v_mov_b32_e32 v14, v13
	s_nop 1
	v_permlane32_swap_b32_e32 v14, v13
	v_add_f32_e32 v13, v13, v14
	s_waitcnt lgkmcnt(4)
	v_mul_f32_e32 v15, v97, v225
	v_fmac_f32_e32 v15, v96, v224
	v_mul_f32_e32 v16, v99, v227
	v_fmac_f32_e32 v16, v98, v226
	v_add_f32_e32 v15, v15, v16
	ds_read_b128 v[220:223], v133 offset:62464
	v_add_f32_e32 v15, 0, v15
	s_waitcnt lgkmcnt(5)
	s_nop 0
	s_nop 0
	s_waitcnt lgkmcnt(4)
	v_mul_f32_e32 v17, v93, v229
	v_fmac_f32_e32 v17, v92, v228
	v_mul_f32_e32 v16, v95, v231
	v_fmac_f32_e32 v16, v94, v230
	v_add_f32_e32 v16, v17, v16
	v_add_f32_e32 v15, v15, v16
	ds_read_b128 v[224:227], v133 offset:63488
	s_waitcnt lgkmcnt(5)
	s_nop 0
	s_nop 0
	s_waitcnt lgkmcnt(4)
	v_mul_f32_e32 v17, v89, v209
	v_fmac_f32_e32 v17, v88, v208
	v_mul_f32_e32 v16, v91, v211
	v_fmac_f32_e32 v16, v90, v210
	v_add_f32_e32 v16, v17, v16
	v_add_f32_e32 v15, v15, v16
	ds_read_b128 v[228:231], v133 offset:64512
	s_waitcnt lgkmcnt(5)
	s_nop 0
	s_nop 0
	s_waitcnt lgkmcnt(4)
; #define LAS __attribute__((address_space(3)))
; __device__ __forceinline__ void phase_norm_route(const bf16_t* x, const float* g, const float* router, bf16_t* H, int* tok_info, unsigned* cnt, LAS unsigned char* lds, int tid, int wid, int lane) {
;     ...
;             float lg[8];
; #pragma unroll
;             for (int e = 0; e < 8; ++e) { float s = 0.f;
; #pragma unroll
;                 for (int j = 0; j < 8; ++j) { const f32x4 r = *(const LAS f32x4*)(RT + e * 2048 + 4 * lane + 256 * j); s += (v[j][0] * r[0] + v[j][1] * r[1]) + (v[j][2] * r[2] + v[j][3] * r[3]); }
;                 lg[e] = wave_sum(s); }
;             int e1 = 0; float l1 = lg[0];
; #pragma unroll
;             for (int e = 1; e < 8; ++e) if (lg[e] > l1) { l1 = lg[e]; e1 = e; }
;             int e2 = -1; float l2 = -__builtin_inff();
; #pragma unroll
;             for (int e = 0; e < 8; ++e) if (e != e1 && lg[e] > l2) { l2 = lg[e]; e2 = e; }
;             if (lane == 0) {
;                 const float ex = __expf(l2 - l1); const float g1 = 1.0f / (1.0f + ex), g2 = ex / (1.0f + ex);
;                 const int r1 = (int)atomicAdd((unsigned*)(LC + e1), 1u); const int r2 = (int)atomicAdd((unsigned*)(LC + e2), 1u);
;                 LAS int* ti = TI + tl * 8; ti[0] = e1; ti[1] = r1; ti[2] = e2; ti[3] = r2; ti[4] = __float_as_int(g1); ti[5] = __float_as_int(g2);
;             }
	v_mul_f32_e32 v17, v85, v213
	v_fmac_f32_e32 v17, v84, v212
	v_mul_f32_e32 v16, v87, v215
	v_fmac_f32_e32 v16, v86, v214
	v_add_f32_e32 v16, v17, v16
	v_add_f32_e32 v15, v15, v16
	s_waitcnt lgkmcnt(4)
	s_nop 0
	s_nop 0
	s_waitcnt lgkmcnt(3)
	v_mul_f32_e32 v17, v81, v217
	v_fmac_f32_e32 v17, v80, v216
	v_mul_f32_e32 v16, v83, v219
	v_fmac_f32_e32 v16, v82, v218
	v_add_f32_e32 v16, v17, v16
	v_add_f32_e32 v15, v15, v16
	s_waitcnt lgkmcnt(3)
	s_nop 0
	s_nop 0
	s_waitcnt lgkmcnt(2)
	v_mul_f32_e32 v17, v77, v221
	v_fmac_f32_e32 v17, v76, v220
	v_mul_f32_e32 v16, v79, v223
	v_fmac_f32_e32 v16, v78, v222
	v_add_f32_e32 v16, v17, v16
	v_add_f32_e32 v15, v15, v16
	s_waitcnt lgkmcnt(1)
	v_mul_f32_e32 v17, v73, v225
	v_fmac_f32_e32 v17, v72, v224
	v_mul_f32_e32 v16, v75, v227
	v_fmac_f32_e32 v16, v74, v226
	v_add_f32_e32 v16, v17, v16
	v_add_f32_e32 v15, v15, v16
	s_waitcnt lgkmcnt(0)
	v_mul_f32_e32 v17, v69, v229
	v_fmac_f32_e32 v17, v68, v228
	v_mul_f32_e32 v16, v71, v231
	v_fmac_f32_e32 v16, v70, v230
	v_add_f32_e32 v16, v17, v16
	v_add_f32_e32 v15, v15, v16
	s_nop 1
	v_add_f32_dpp v15, v15, v15 quad_perm:[1,0,3,2] row_mask:0xf bank_mask:0xf
	s_nop 1
	v_add_f32_dpp v15, v15, v15 quad_perm:[2,3,0,1] row_mask:0xf bank_mask:0xf
	s_nop 1
	v_add_f32_dpp v15, v15, v15 row_half_mirror row_mask:0xf bank_mask:0xf
	s_nop 1
	v_add_f32_dpp v15, v15, v15 row_mirror row_mask:0xf bank_mask:0xf
	v_mov_b32_e32 v16, v15
	s_nop 1
	v_permlane16_swap_b32_e32 v16, v15
	v_add_f32_e32 v15, v15, v16
	v_mov_b32_e32 v16, v15
	s_nop 1
	v_permlane32_swap_b32_e32 v16, v15
	v_add_f32_e32 v15, v15, v16
	s_waitcnt lgkmcnt(0)
	s_nop 0
	s_nop 0
	s_waitcnt lgkmcnt(0)
	s_nop 0
	s_nop 0
	s_waitcnt lgkmcnt(0)
	s_nop 0
	s_nop 0
	s_waitcnt lgkmcnt(0)
	s_nop 0
	s_nop 0
	s_waitcnt lgkmcnt(0)
	s_nop 0
	s_nop 0
	s_and_saveexec_b64 s[30:31], s[2:3]
	s_cbranch_execz .LBB0_2698
	s_nop 0
	s_nop 0
	v_cmp_gt_f32_e32 vcc, v0, v1
	s_nop 0
	s_nop 0
	v_cndmask_b32_e32 v4, v1, v0, vcc
	v_cmp_gt_f32_e64 s[8:9], v2, v4
	s_nop 0
	s_nop 0
	v_cndmask_b32_e64 v4, v4, v2, s[8:9]
	v_cmp_gt_f32_e64 s[10:11], v7, v4
	s_waitcnt lgkmcnt(0)
	s_nop 0
	s_mov_b32 s20, 0xff800000
	v_cndmask_b32_e64 v4, v4, v7, s[10:11]
	v_cmp_gt_f32_e64 s[12:13], v9, v4
	v_cmp_nlg_f32_e64 s[20:21], s20, v1
	s_nop 0
	v_cndmask_b32_e64 v4, v4, v9, s[12:13]
	v_cmp_gt_f32_e64 s[14:15], v11, v4
	s_nop 1
	v_cndmask_b32_e64 v4, v4, v11, s[14:15]
	v_cmp_gt_f32_e64 s[16:17], v13, v4
	s_nop 1
	v_cndmask_b32_e64 v5, v4, v13, s[16:17]
	v_cndmask_b32_e64 v4, 0, 1, vcc
	v_cndmask_b32_e64 v4, v4, 2, s[8:9]
	v_cndmask_b32_e64 v4, v4, 3, s[10:11]
	v_cndmask_b32_e64 v4, v4, 4, s[12:13]
	v_cndmask_b32_e64 v4, v4, 5, s[14:15]
	v_cndmask_b32_e64 v4, v4, 6, s[16:17]
	v_cmp_ngt_f32_e32 vcc, v15, v5
	s_and_b64 s[22:23], s[16:17], vcc
	s_nop 0
	v_cndmask_b32_e32 v4, 7, v4, vcc
	v_cmp_eq_u32_e64 s[18:19], 0, v4
	s_or_b64 s[18:19], s[18:19], s[20:21]
	v_cmp_ne_u32_e64 s[16:17], 1, v4
	v_cndmask_b32_e64 v1, v1, v203, s[18:19]
	v_cmp_gt_f32_e64 s[20:21], v0, v1
	s_and_b64 s[16:17], s[16:17], s[20:21]
	v_cndmask_b32_e64 v0, v1, v0, s[16:17]
	v_cmp_ne_u32_e64 s[14:15], 2, v4
	v_cmp_gt_f32_e64 s[20:21], v2, v0
	s_and_b64 s[14:15], s[14:15], s[20:21]
	v_cndmask_b32_e64 v0, v0, v2, s[14:15]
	v_cmp_ne_u32_e64 s[12:13], 3, v4
	v_cmp_gt_f32_e64 s[20:21], v7, v0
	s_and_b64 s[12:13], s[12:13], s[20:21]
	v_cndmask_b32_e64 v0, v0, v7, s[12:13]
	v_cmp_ne_u32_e64 s[10:11], 4, v4
	v_cmp_gt_f32_e64 s[20:21], v9, v0
	s_and_b64 s[10:11], s[10:11], s[20:21]
	v_cndmask_b32_e64 v0, v0, v9, s[10:11]
	v_cmp_ne_u32_e64 s[8:9], 5, v4
	v_cmp_gt_f32_e64 s[20:21], v11, v0
	s_and_b64 s[8:9], s[8:9], s[20:21]
	v_cndmask_b32_e64 v0, v0, v11, s[8:9]
	v_cmp_ngt_f32_e64 s[20:21], v13, v0
	s_or_b64 s[20:21], s[22:23], s[20:21]
	v_cndmask_b32_e64 v1, 0, -1, s[18:19]
	v_cndmask_b32_e64 v0, v13, v0, s[20:21]
	v_cmp_gt_f32_e64 s[22:23], v15, v0
	s_and_b64 s[22:23], vcc, s[22:23]
	v_cndmask_b32_e64 v1, v1, 1, s[16:17]
	v_cndmask_b32_e64 v0, v0, v15, s[22:23]
	v_cndmask_b32_e32 v2, v15, v5, vcc
	v_cndmask_b32_e64 v1, v1, 2, s[14:15]
	v_sub_f32_e32 v0, v0, v2
	v_cndmask_b32_e64 v1, v1, 3, s[12:13]
	v_mul_f32_e32 v0, 0x3fb8aa3b, v0
	v_cndmask_b32_e64 v1, v1, 4, s[10:11]
	v_exp_f32_e32 v0, v0
	v_cndmask_b32_e64 v1, v1, 5, s[8:9]
	v_cndmask_b32_e64 v1, 6, v1, s[20:21]
	v_cndmask_b32_e64 v6, v1, 7, s[22:23]
	v_lshl_add_u32 v1, v4, 2, s34
	v_add_f32_e32 v2, 1.0, v0
	ds_add_rtn_u32 v5, v1, v188
	v_lshl_add_u32 v1, v6, 2, s34
	ds_add_rtn_u32 v7, v1, v188
	v_div_scale_f32 v1, s[8:9], v2, v2, v0
	v_rcp_f32_e32 v8, v1
	s_add_i32 s10, s35, s38
	s_add_i32 s11, s10, 0x10000
	v_mov_b32_e32 v9, s11
	s_waitcnt lgkmcnt(0)
	ds_write_b128 v9, v[4:7]
	v_fma_f32 v4, -v1, v8, 1.0
	v_fmac_f32_e32 v8, v4, v8
	v_div_scale_f32 v4, vcc, v0, v2, v0
	v_mul_f32_e32 v5, v4, v8
	v_fma_f32 v6, -v1, v5, v4
	v_fmac_f32_e32 v5, v6, v8
	v_fma_f32 v1, -v1, v5, v4
	v_div_scale_f32 v4, s[8:9], v2, v2, 1.0
	v_rcp_f32_e32 v6, v4
	v_div_fmas_f32 v1, v1, v8, v5
	v_div_fixup_f32 v1, v1, v2, v0
	s_add_i32 s10, s10, 0x10010
	v_fma_f32 v0, -v4, v6, 1.0
	v_fmac_f32_e32 v6, v0, v6
	v_div_scale_f32 v0, vcc, 1.0, v2, 1.0
	v_mul_f32_e32 v5, v0, v6
	v_fma_f32 v7, -v4, v5, v0
	v_fmac_f32_e32 v5, v7, v6
	v_fma_f32 v0, -v4, v5, v0
	v_div_fmas_f32 v0, v0, v6, v5
	v_div_fixup_f32 v0, v0, v2, 1.0
	v_mov_b32_e32 v2, s10
	ds_write_b64 v2, v[0:1]
	s_branch .LBB0_2698

; __device__ __forceinline__ void phase_gather(const bf16_t* H, bf16_t* HS, int* tok_info, float* rowgate, const unsigned* cnt, int wid, int lane) {
;     ...
;     for (int t0 = gw; t0 < T; t0 += NB * NGW) {
;         u32x4 w[NB][2]; int d1[NB], d2[NB], g1[NB], g2[NB];
; #pragma unroll
;         for (int b = 0; b < NB; ++b) { const int t = t0 + b * NGW, tc = t < T ? t : T - 1;
;             const int* ti = tok_info + (size_t)tc * 8;
;             const int e1 = ti[0], p1 = ti[1], e2 = ti[2], p2 = ti[3]; g1[b] = ti[4]; g2[b] = ti[5];
;             int o1 = 0, o2 = 0;
; #pragma unroll
;             for (int e = 0; e < 8; ++e) { o1 = (e == e1) ? toff[e] : o1; o2 = (e == e2) ? toff[e] : o2; }
;             d1[b] = o1 * 256 + p1; d2[b] = o2 * 256 + p2;
;             const u32x4* src = (const u32x4*)((const unsigned char*)H + (size_t)tc * D);
;             w[b][0] = src[lane]; w[b][1] = src[lane + 64]; }
; #pragma unroll
;         for (int b = 0; b < NB; ++b) { const int t = t0 + b * NGW; if (t < T) {
;             u32x4* q1 = (u32x4*)((unsigned char*)HS + (size_t)d1[b] * D); u32x4* q2 = (u32x4*)((unsigned char*)HS + (size_t)d2[b] * D);
;             q1[lane] = w[b][0]; q1[lane + 64] = w[b][1]; q2[lane] = w[b][0]; q2[lane + 64] = w[b][1];
;             if (lane == 0) { int* ti = tok_info + (size_t)t * 8; ti[6] = d1[b]; ti[7] = d2[b]; rowgate[d1[b]] = __int_as_float(g1[b]); rowgate[d2[b]] = __int_as_float(g2[b]); } } }
.LBB0_2766:
	s_add_u32 s10, s7, s4
	s_addc_u32 s11, s37, s5
	v_mov_b32_e32 v2, 0x69492000
	global_load_dwordx4 v[4:7], v2, s[10:11]
	s_add_u32 s2, s10, 0x69492000
	s_addc_u32 s3, s11, 0
	global_load_dwordx2 v[40:41], v3, s[2:3] offset:16
	v_readlane_b32 s66, v254, 33
	s_add_i32 s66, s66, s6
	s_min_i32 s66, s66, 0x3fff
	s_ashr_i32 s67, s66, 31
	s_lshl_b64 s[66:67], s[66:67], 5
	s_add_u32 s60, s0, s66
	s_addc_u32 s61, s20, s67
	v_readlane_b32 s66, v253, 40
	s_add_i32 s66, s66, s6
	s_min_i32 s66, s66, 0x3fff
	s_ashr_i32 s67, s66, 31
	s_lshl_b64 s[66:67], s[66:67], 5
	s_add_u32 s62, s0, s66
	s_addc_u32 s63, s20, s67
	v_readlane_b32 s66, v253, 42
	s_add_i32 s66, s66, s6
	s_min_i32 s66, s66, 0x3fff
	s_ashr_i32 s67, s66, 31
	s_lshl_b64 s[66:67], s[66:67], 5
	s_add_u32 s64, s0, s66
	s_addc_u32 s65, s20, s67
	global_load_dwordx2 v[208:209], v3, s[60:61] offset:16
	global_load_dwordx4 v[212:215], v3, s[60:61]
	global_load_dwordx2 v[216:217], v3, s[62:63] offset:16
	global_load_dwordx4 v[220:223], v3, s[62:63]
	global_load_dwordx2 v[224:225], v3, s[64:65] offset:16
	global_load_dwordx4 v[228:231], v3, s[64:65]
	s_waitcnt vmcnt(7)
	v_readfirstlane_b32 s12, v6
	v_readfirstlane_b32 s13, v4
	s_cmp_eq_u32 s12, 1
	s_cselect_b32 s2, s36, 0
	s_cmp_eq_u32 s13, 1
	s_cselect_b32 s3, s21, 0
	s_cmp_eq_u32 s13, 2
	s_cselect_b32 s3, s22, s3
	s_cmp_eq_u32 s12, 2
	s_cselect_b32 s2, s35, s2
	s_cmp_eq_u32 s12, 3
	s_cselect_b32 s2, s34, s2
	s_cmp_eq_u32 s13, 3
	s_cselect_b32 s3, s23, s3
	s_cmp_eq_u32 s13, 4
	s_cselect_b32 s3, s24, s3
	s_cmp_eq_u32 s12, 4
	s_cselect_b32 s2, s31, s2
	s_cmp_eq_u32 s12, 5
	s_cselect_b32 s2, s30, s2
	s_cmp_eq_u32 s13, 5
	s_cselect_b32 s3, s25, s3
	s_cmp_eq_u32 s13, 6
	s_cselect_b32 s3, s26, s3
	s_cmp_eq_u32 s12, 6
	s_cselect_b32 s2, s29, s2
	s_cmp_eq_u32 s12, 7
	s_cselect_b32 s2, s28, s2
	s_cmp_eq_u32 s13, 7
	s_cselect_b32 s3, s27, s3
	s_lshl_b32 s3, s3, 8
	s_lshl_b32 s2, s2, 8
	v_add_u32_e32 v44, s2, v7
	v_add_u32_e32 v42, s3, v5
	v_lshl_add_u64 v[4:5], v[38:39], 0, s[4:5]
	s_mov_b32 s2, 0x60c92000
	v_add_co_u32_e64 v4, s[2:3], s2, v4
	v_readlane_b32 s12, v253, 42
	s_nop 0
	v_addc_co_u32_e64 v5, s[2:3], 0, v5, s[2:3]
	v_readlane_b32 s2, v254, 33
	s_add_i32 s14, s2, s6
	s_min_i32 s16, s14, 0x3fff
	v_readlane_b32 s3, v254, 34
	s_ashr_i32 s17, s16, 31
	s_lshl_b64 s[2:3], s[16:17], 5
	s_add_u32 s18, s0, s2
	s_addc_u32 s19, s20, s3
	global_load_dwordx4 v[8:11], v[4:5], off
	s_nop 0
	global_load_dwordx4 v[4:7], v[4:5], off offset:1024
	v_readlane_b32 s2, v253, 40
	s_nop 0
	s_lshl_b64 s[16:17], s[16:17], 11
	s_add_i32 s2, s2, s6
	v_ashrrev_i32_e32 v43, 31, v42
	v_lshlrev_b64 v[46:47], 11, v[42:43]
	v_ashrrev_i32_e32 v45, 31, v44
	v_lshlrev_b64 v[48:49], 11, v[44:45]
	v_lshl_add_u64 v[46:47], v[36:37], 0, v[46:47]
	s_waitcnt vmcnt(7)
	v_readfirstlane_b32 s3, v209
	v_readfirstlane_b32 s13, v208
	s_nop 0
	s_waitcnt vmcnt(6)
	v_readfirstlane_b32 s19, v213
	v_readfirstlane_b32 s44, v212
	v_lshl_add_u64 v[12:13], v[0:1], 0, s[16:17]
	s_min_i32 s16, s2, 0x3fff
	s_ashr_i32 s17, s16, 31
	s_lshl_b64 s[38:39], s[16:17], 5
	s_add_u32 s38, s0, s38
	s_addc_u32 s39, s20, s39
	global_load_dwordx4 v[20:23], v[12:13], off
	global_load_dwordx4 v[24:27], v[12:13], off offset:1024
	v_readfirstlane_b32 s15, v215
	s_nop 0
	v_readfirstlane_b32 s18, v214
	s_lshl_b64 s[16:17], s[16:17], 11
	s_add_i32 s12, s12, s6
	s_waitcnt vmcnt(7)
	v_readfirstlane_b32 s40, v217
	v_readfirstlane_b32 s41, v216
	s_nop 0
	s_waitcnt vmcnt(6)
	v_readfirstlane_b32 s43, v221
	v_readfirstlane_b32 s48, v220
	v_lshl_add_u64 v[12:13], v[0:1], 0, s[16:17]
	s_min_i32 s16, s12, 0x3fff
	s_ashr_i32 s17, s16, 31
	s_lshl_b64 s[38:39], s[16:17], 5
	s_add_u32 s50, s0, s38
	s_addc_u32 s51, s20, s39
	global_load_dwordx4 v[28:31], v[12:13], off
	global_load_dwordx4 v[32:35], v[12:13], off offset:1024
	v_readfirstlane_b32 s42, v223
	s_nop 0
	v_readfirstlane_b32 s47, v222
	s_lshl_b64 s[16:17], s[16:17], 11
	v_lshl_add_u64 v[16:17], v[0:1], 0, s[16:17]
	s_waitcnt vmcnt(7)
	v_readfirstlane_b32 s38, v225
	v_readfirstlane_b32 s39, v224
	s_nop 0
	s_waitcnt vmcnt(0)
	v_readfirstlane_b32 s45, v231
	v_readfirstlane_b32 s49, v230
	v_readfirstlane_b32 s46, v229
	v_readfirstlane_b32 s50, v228
	global_load_dwordx4 v[12:15], v[16:17], off
	s_nop 0
	global_load_dwordx4 v[16:19], v[16:17], off offset:1024
	s_nop 0
	global_store_dwordx4 v[46:47], v[8:11], off
	global_store_dwordx4 v[46:47], v[4:7], off offset:1024
	v_lshl_add_u64 v[46:47], v[36:37], 0, v[48:49]
	global_store_dwordx4 v[46:47], v[8:11], off
	global_store_dwordx4 v[46:47], v[4:7], off offset:1024
	s_and_saveexec_b64 s[16:17], vcc
	s_cbranch_execz .LBB0_2772
	v_mov_b32_e32 v4, v42
	v_mov_b32_e32 v5, v44
	v_lshlrev_b64 v[6:7], 2, v[44:45]
	v_lshlrev_b64 v[8:9], 2, v[42:43]
	v_mov_b32_e32 v2, 0x69492000
	v_lshl_add_u64 v[6:7], s[8:9], 0, v[6:7]
	v_lshl_add_u64 v[8:9], s[8:9], 0, v[8:9]
	global_store_dwordx2 v2, v[4:5], s[10:11] offset:24
	global_store_dword v[8:9], v40, off
	global_store_dword v[6:7], v41, off
	s_or_b64 exec, exec, s[16:17]
	s_cmpk_gt_i32 s14, 0x3fff
	s_cbranch_scc0 .LBB0_2773
